# f24 plus proj Q/K epilogue tail edits (DPP emax reduction, sum(va) butterfly only in workgroups 0-7)
# baseline (speedup 1.0000x reference)
_Z11proj_kernelPKfS0_S0_S0_S0_S0_S0_S0_S0_S0_S0_S0_S0_PfS1_PDF16_S1_S0_S0_S2_:
	s_mov_b32 s88, s2
	s_load_dwordx2 s[16:17], s[0:1], 0x90
	s_load_dwordx4 s[4:7], s[0:1], 0x80
	s_cmpk_gt_u32 s2, 0x5f
	s_mov_b64 s[8:9], -1
	s_cbranch_scc0 .LBB0_16
	s_load_dwordx4 s[8:11], s[0:1], 0x58
	s_lshr_b32 s3, s2, 3
	s_cmpk_gt_u32 s2, 0xbf
	s_mov_b64 s[12:13], -1
	s_cbranch_scc0 .LBB0_3
	v_lshlrev_b32_e32 v54, 2, v0
	v_mov_b32_e32 v55, 0
	s_waitcnt lgkmcnt(0)
	v_lshl_add_u64 v[2:3], s[6:7], 0, v[54:55]
	v_lshl_add_u64 v[4:5], s[16:17], 0, v[54:55]
	v_cmp_gt_u32_e32 vcc, 64, v0
	s_load_dwordx4 s[12:15], s[0:1], 0x38
	s_load_dwordx2 s[22:23], s[0:1], 0x10
	v_cndmask_b32_e32 v2, v4, v2, vcc
	v_cndmask_b32_e32 v3, v5, v3, vcc
	global_load_dword v70, v[2:3], off
	v_lshrrev_b32_e32 v2, 2, v0
	v_and_b32_e32 v56, 15, v0
	v_and_b32_e32 v18, 48, v2
	v_or_b32_e32 v68, v18, v56
	v_bfe_u32 v1, v0, 4, 2
	v_lshlrev_b32_e32 v2, 8, v68
	v_mov_b32_e32 v3, v55
	s_lshl_b32 s20, s2, 1
	v_lshl_add_u64 v[2:3], s[8:9], 0, v[2:3]
	v_lshlrev_b32_e32 v4, 5, v1
	v_mov_b32_e32 v5, v55
	s_and_b32 s20, s20, 6
	s_bfe_u32 s21, s2, 0x10003
	v_lshl_add_u64 v[14:15], v[2:3], 0, v[4:5]
	s_sub_i32 s19, s3, 24
	s_or_b32 s21, s21, s20
	v_lshl_add_u64 v[6:7], v[14:15], 0, 16
	s_mov_b64 s[24:25], 0x80
	s_bfe_u32 s18, s2, 0x10002
	s_lshr_b32 s19, s19, 1
	s_lshl_b32 s20, s21, 6
	v_lshl_add_u64 v[10:11], v[14:15], 0, s[24:25]
	s_mov_b64 s[24:25], 0x90
	v_lshlrev_b32_e32 v22, 2, v18
	v_mov_b32_e32 v23, v55
	s_lshl_b32 s21, s21, 8
	v_lshl_add_u64 v[14:15], v[14:15], 0, s[24:25]
	v_lshl_add_u64 v[24:25], s[10:11], 0, v[22:23]
	v_lshlrev_b32_e32 v18, 4, v1
	v_mov_b32_e32 v19, v55
	s_waitcnt lgkmcnt(0)
	s_add_u32 s14, s14, s21
	v_lshl_add_u64 v[18:19], v[24:25], 0, v[18:19]
	s_addc_u32 s15, s15, 0
	v_lshlrev_b32_e32 v26, 2, v56
	v_mov_b32_e32 v27, v55
	v_lshl_add_u64 v[22:23], s[14:15], 0, v[22:23]
	s_mul_i32 s26, s18, 0x180
	v_lshrrev_b32_e32 v57, 4, v0
	v_lshl_add_u64 v[24:25], v[24:25], 0, v[26:27]
	v_lshl_add_u64 v[22:23], v[22:23], 0, v[26:27]
	s_mulk_i32 s19, 0x60
	global_load_dword v69, v[22:23], off
	v_or_b32_e32 v22, s26, v57
	v_add_u32_e32 v22, s19, v22
	v_mov_b32_e32 v23, v55
	v_lshlrev_b64 v[22:23], 11, v[22:23]
	v_and_b32_e32 v72, 60, v54
	v_lshl_add_u64 v[22:23], s[22:23], 0, v[22:23]
	v_lshlrev_b32_e32 v54, 2, v72
	v_lshl_add_u64 v[66:67], v[22:23], 0, v[54:55]
	global_load_dwordx4 v[22:25], v[66:67], off
	s_mov_b32 s14, 0x10000
	v_add_co_u32_e32 v64, vcc, s14, v66
	s_mov_b32 s15, 0x20000
	s_nop 0
	v_addc_co_u32_e32 v65, vcc, 0, v67, vcc
	global_load_dwordx4 v[30:33], v[64:65], off
	v_add_co_u32_e32 v62, vcc, s15, v66
	v_or_b32_e32 v26, s20, v57
	s_nop 0
	v_addc_co_u32_e32 v63, vcc, 0, v67, vcc
	global_load_dwordx4 v[34:37], v[62:63], off
	v_lshlrev_b32_e32 v26, 9, v26
	v_lshl_add_u64 v[26:27], v[26:27], 2, s[12:13]
	v_lshl_add_u64 v[60:61], v[26:27], 0, v[54:55]
	v_add_co_u32_e32 v58, vcc, s14, v60
	global_load_dwordx4 v[38:41], v[60:61], off
	s_nop 0
	v_addc_co_u32_e32 v59, vcc, 0, v61, vcc
	global_load_dwordx4 v[42:45], v[58:59], off
	global_load_dwordx4 v[46:49], v[66:67], off offset:256
	global_load_dwordx4 v[50:53], v[64:65], off offset:256
	global_load_dwordx4 v[74:77], v[62:63], off offset:256
	global_load_dwordx4 v[78:81], v[60:61], off offset:256
	global_load_dwordx4 v[82:85], v[58:59], off offset:256
	global_load_dwordx4 v[86:89], v[66:67], off offset:512
	global_load_dwordx4 v[90:93], v[64:65], off offset:512
	v_lshrrev_b32_e32 v26, 8, v0
	v_mul_u32_u24_e32 v54, 48, v26
	global_load_dwordx4 v[26:29], v[62:63], off offset:512
	global_load_dwordx4 v[94:97], v[60:61], off offset:512
	v_or_b32_e32 v102, v54, v56
	v_and_b32_e32 v56, 48, v0
	s_movk_i32 s14, 0xa0
	v_mad_u32_u24 v73, v68, s14, v56
	v_lshl_or_b32 v1, v1, 2, v54
	v_mul_lo_u32 v1, v1, s14
	v_lshl_add_u32 v1, v68, 1, v1
	s_movk_i32 s15, 0x180
	s_waitcnt vmcnt(13)
	v_cvt_f16_f32_e32 v22, v22
	v_cvt_f16_f32_e32 v25, v25
	v_cvt_pk_f16_f32 v23, v23, v24
	v_mul_u32_u24_e32 v24, 0xa0, v57
	v_pack_b32_f16 v22, v22, v23
	v_alignbit_b32 v23, v25, v23, 16
	v_lshl_add_u32 v72, v72, 1, v24
	s_waitcnt vmcnt(12)
	v_cvt_f16_f32_e32 v25, v30
	v_cvt_f16_f32_e32 v30, v33
	v_cvt_pk_f16_f32 v31, v31, v32
	v_mad_u64_u32 v[56:57], s[12:13], v102, s14, v[56:57]
	v_pack_b32_f16 v24, v25, v31
	v_alignbit_b32 v25, v30, v31, 16
	s_waitcnt vmcnt(11)
	v_cvt_f16_f32_e32 v30, v34
	ds_write2st64_b64 v72, v[22:23], v[24:25] offset1:10
	s_waitcnt vmcnt(8)
	v_cvt_f16_f32_e32 v34, v46
	v_cvt_pk_f16_f32 v23, v35, v36
	v_cvt_f16_f32_e32 v35, v49
	v_cvt_pk_f16_f32 v36, v47, v48
	v_pack_b32_f16 v102, v34, v36
	s_waitcnt vmcnt(7)
	v_cvt_f16_f32_e32 v34, v50
	v_alignbit_b32 v103, v35, v36, 16
	v_cvt_f16_f32_e32 v35, v53
	v_cvt_pk_f16_f32 v36, v51, v52
	v_pack_b32_f16 v104, v34, v36
	s_waitcnt vmcnt(6)
	v_cvt_f16_f32_e32 v34, v74
	v_alignbit_b32 v105, v35, v36, 16
	v_cvt_f16_f32_e32 v35, v77
	v_cvt_pk_f16_f32 v36, v75, v76
	v_pack_b32_f16 v106, v34, v36
	s_waitcnt vmcnt(5)
	v_cvt_f16_f32_e32 v34, v78
	v_alignbit_b32 v107, v35, v36, 16
	v_cvt_f16_f32_e32 v35, v81
	v_cvt_pk_f16_f32 v36, v79, v80
	v_pack_b32_f16 v108, v34, v36
	s_waitcnt vmcnt(4)
	v_cvt_f16_f32_e32 v34, v82
	v_cvt_f16_f32_e32 v24, v37
	v_pack_b32_f16 v22, v30, v23
	v_cvt_f16_f32_e32 v25, v38
	v_cvt_f16_f32_e32 v30, v41
	v_alignbit_b32 v109, v35, v36, 16
	v_cvt_f16_f32_e32 v35, v85
	v_cvt_pk_f16_f32 v36, v83, v84
	v_cvt_pk_f16_f32 v31, v39, v40
	v_pack_b32_f16 v110, v34, v36
	s_waitcnt vmcnt(3)
	v_cvt_f16_f32_e32 v34, v86
	v_alignbit_b32 v23, v24, v23, 16
	v_pack_b32_f16 v24, v25, v31
	v_alignbit_b32 v25, v30, v31, 16
	v_cvt_f16_f32_e32 v30, v42
	v_cvt_f16_f32_e32 v31, v45
	v_alignbit_b32 v111, v35, v36, 16
	v_cvt_pk_f16_f32 v36, v87, v88
	v_cvt_pk_f16_f32 v32, v43, v44
	v_cvt_f16_f32_e32 v35, v89
	v_pack_b32_f16 v114, v34, v36
	s_waitcnt vmcnt(2)
	v_cvt_f16_f32_e32 v34, v90
	v_pack_b32_f16 v30, v30, v32
	v_alignbit_b32 v31, v31, v32, 16
	ds_write2st64_b64 v72, v[22:23], v[24:25] offset0:20 offset1:60
	global_load_dwordx4 v[22:25], v[58:59], off offset:512
	ds_write_b64 v72, v[30:31] offset:35840
	s_waitcnt lgkmcnt(0)
	s_barrier
	global_load_dwordx4 v[30:33], v[66:67], off offset:768
	global_load_dwordx4 v[98:101], v[64:65], off offset:768
	v_cvt_pk_f16_f32 v39, v91, v92
	v_alignbit_b32 v115, v35, v36, 16
	v_cvt_f16_f32_e32 v38, v93
	v_pack_b32_f16 v116, v34, v39
	ds_read_b128 v[34:37], v56
	s_waitcnt vmcnt(4)
	v_cvt_f16_f32_e32 v57, v26
	v_alignbit_b32 v117, v38, v39, 16
	ds_read_b128 v[38:41], v56 offset:2560
	ds_read_b128 v[46:49], v73 offset:30720
	ds_read_b128 v[50:53], v56 offset:5120
	ds_read_b128 v[74:77], v56 offset:64
	ds_read_b128 v[78:81], v73 offset:30784
	v_cvt_f16_f32_e32 v87, v29
	s_waitcnt lgkmcnt(3)
	v_mfma_f32_16x16x32_f16 v[34:37], v[34:37], v[46:49], 0
	v_cvt_pk_f16_f32 v86, v27, v28
	global_load_dwordx4 v[42:45], v[62:63], off offset:768
	ds_read_b128 v[26:29], v56 offset:2624
	v_mfma_f32_16x16x32_f16 v[82:85], v[38:41], v[46:49], 0
	v_pack_b32_f16 v118, v57, v86
	v_alignbit_b32 v119, v87, v86, 16
	ds_read_b128 v[86:89], v56 offset:5184
	s_waitcnt lgkmcnt(4)
	v_mfma_f32_16x16x32_f16 v[50:53], v[50:53], v[46:49], 0
	global_load_dwordx4 v[46:49], v[60:61], off offset:768
	ds_write2st64_b64 v72, v[102:103], v[104:105] offset0:30 offset1:40
	ds_write2st64_b64 v72, v[106:107], v[108:109] offset0:50 offset1:80
	ds_write_b64 v72, v[110:111] offset:46080
	s_waitcnt lgkmcnt(5)
	v_mfma_f32_16x16x32_f16 v[74:77], v[74:77], v[78:81], v[34:37]
	s_waitcnt vmcnt(5)
	v_cvt_f16_f32_e32 v57, v94
	v_cvt_f16_f32_e32 v90, v97
	v_cvt_pk_f16_f32 v91, v95, v96
	global_load_dwordx4 v[34:37], v[58:59], off offset:768
	s_waitcnt lgkmcnt(0)
	s_barrier
	global_load_dwordx4 v[38:41], v[66:67], off offset:1024
	v_pack_b32_f16 v120, v57, v91
	v_alignbit_b32 v121, v90, v91, 16
	global_load_dwordx4 v[90:93], v[64:65], off offset:1024
	v_mfma_f32_16x16x32_f16 v[50:53], v[86:89], v[78:81], v[50:53]
	global_load_dwordx4 v[86:89], v[62:63], off offset:1024
	s_load_dwordx2 s[12:13], s[0:1], 0x78
	s_waitcnt vmcnt(8)
	v_cvt_f16_f32_e32 v22, v22
	v_mfma_f32_16x16x32_f16 v[82:85], v[26:29], v[78:81], v[82:85]
	v_cvt_f16_f32_e32 v25, v25
	v_cvt_pk_f16_f32 v23, v23, v24
	v_pack_b32_f16 v122, v22, v23
	s_waitcnt vmcnt(7)
	v_cvt_f16_f32_e32 v26, v30
	v_cvt_pk_f16_f32 v57, v31, v32
	v_alignbit_b32 v123, v25, v23, 16
	ds_read_b128 v[22:25], v56 offset:15360
	ds_read_b128 v[78:81], v73 offset:40960
	v_cvt_f16_f32_e32 v125, v33
	s_waitcnt vmcnt(6)
	v_cvt_f16_f32_e32 v126, v98
	v_cvt_pk_f16_f32 v127, v99, v100
	v_cvt_f16_f32_e32 v128, v101
	ds_read_b128 v[94:97], v56 offset:15424
	ds_read_b128 v[98:101], v73 offset:41024
	ds_read_b128 v[30:33], v56 offset:17920
	ds_read_b128 v[102:105], v56 offset:17984
	ds_read_b128 v[106:109], v56 offset:20480
	ds_read_b128 v[110:113], v56 offset:20544
	ds_write2st64_b64 v72, v[114:115], v[116:117] offset1:10
	global_load_dwordx4 v[114:117], v[60:61], off offset:1024
	v_pack_b32_f16 v124, v26, v57
	global_load_dwordx4 v[26:29], v[58:59], off offset:1024
	s_waitcnt lgkmcnt(0)
	v_mfma_f32_16x16x32_f16 v[74:77], v[22:25], v[78:81], v[74:77]
	ds_write2st64_b64 v72, v[118:119], v[120:121] offset0:20 offset1:60
	s_waitcnt vmcnt(7)
	v_cvt_f16_f32_e32 v42, v42
	v_cvt_f16_f32_e32 v45, v45
	v_mfma_f32_16x16x32_f16 v[82:85], v[30:33], v[78:81], v[82:85]
	ds_write_b64 v72, v[122:123] offset:35840
	s_waitcnt lgkmcnt(0)
	s_barrier
	global_load_dwordx4 v[22:25], v[66:67], off offset:1280
	global_load_dwordx4 v[30:33], v[64:65], off offset:1280
	v_cvt_pk_f16_f32 v43, v43, v44
	v_alignbit_b32 v125, v125, v57, 16
	v_mfma_f32_16x16x32_f16 v[50:53], v[106:109], v[78:81], v[50:53]
	v_pack_b32_f16 v108, v42, v43
	v_alignbit_b32 v109, v45, v43, 16
	s_waitcnt vmcnt(7)
	v_cvt_f16_f32_e32 v34, v34
	v_cvt_pk_f16_f32 v35, v35, v36
	v_cvt_f16_f32_e32 v36, v37
	v_mfma_f32_16x16x32_f16 v[42:45], v[94:97], v[98:101], v[74:77]
	v_cvt_f16_f32_e32 v57, v46
	s_waitcnt vmcnt(6)
	v_cvt_f16_f32_e32 v37, v41
	v_pack_b32_f16 v106, v126, v127
	v_cvt_f16_f32_e32 v74, v49
	v_cvt_pk_f16_f32 v75, v47, v48
	v_mfma_f32_16x16x32_f16 v[46:49], v[102:105], v[98:101], v[82:85]
	v_pack_b32_f16 v104, v34, v35
	v_cvt_f16_f32_e32 v34, v38
	v_alignbit_b32 v105, v36, v35, 16
	v_cvt_pk_f16_f32 v35, v39, v40
	v_alignbit_b32 v119, v37, v35, 16
	v_pack_b32_f16 v118, v34, v35
	ds_read_b128 v[34:37], v56
	v_pack_b32_f16 v102, v57, v75
	v_alignbit_b32 v103, v74, v75, 16
	ds_read_b128 v[74:77], v56 offset:2560
	ds_read_b128 v[78:81], v73 offset:30720
	s_waitcnt vmcnt(5)
	v_cvt_f16_f32_e32 v38, v90
	v_cvt_f16_f32_e32 v40, v93
	v_mfma_f32_16x16x32_f16 v[50:53], v[110:113], v[98:101], v[50:53]
	v_cvt_pk_f16_f32 v39, v91, v92
	v_pack_b32_f16 v120, v38, v39
	v_alignbit_b32 v121, v40, v39, 16
	ds_read_b128 v[82:85], v56 offset:5120
	ds_read_b128 v[90:93], v56 offset:64
	ds_read_b128 v[94:97], v73 offset:30784
	s_waitcnt lgkmcnt(3)
	v_mfma_f32_16x16x32_f16 v[34:37], v[34:37], v[78:81], v[42:45]
	global_load_dwordx4 v[38:41], v[62:63], off offset:1280
	v_alignbit_b32 v107, v128, v127, 16
	ds_read_b128 v[98:101], v56 offset:2624
	s_waitcnt vmcnt(5)
	v_cvt_f16_f32_e32 v42, v86
	v_cvt_f16_f32_e32 v44, v89
	v_mfma_f32_16x16x32_f16 v[74:77], v[74:77], v[78:81], v[46:49]
	v_cvt_pk_f16_f32 v43, v87, v88
	v_pack_b32_f16 v122, v42, v43
	v_alignbit_b32 v123, v44, v43, 16
	s_waitcnt lgkmcnt(3)
	v_mfma_f32_16x16x32_f16 v[78:81], v[82:85], v[78:81], v[50:53]
	global_load_dwordx4 v[42:45], v[58:59], off offset:1280
	ds_read_b128 v[86:89], v56 offset:5184
	ds_write2st64_b64 v72, v[124:125], v[106:107] offset0:30 offset1:40
	global_load_dwordx4 v[50:53], v[60:61], off offset:1280
	ds_write2st64_b64 v72, v[108:109], v[102:103] offset0:50 offset1:80
	ds_write_b64 v72, v[104:105] offset:46080
	s_waitcnt lgkmcnt(0)
	s_barrier
	global_load_dwordx4 v[46:49], v[66:67], off offset:1536
	global_load_dwordx4 v[82:85], v[64:65], off offset:1536
	v_mfma_f32_16x16x32_f16 v[78:81], v[86:89], v[94:97], v[78:81]
	ds_read_b128 v[86:89], v73 offset:40960
	s_waitcnt vmcnt(8)
	v_cvt_f16_f32_e32 v57, v114
	v_mfma_f32_16x16x32_f16 v[34:37], v[90:93], v[94:97], v[34:37]
	s_waitcnt vmcnt(7)
	v_cvt_f16_f32_e32 v26, v26
	v_cvt_f16_f32_e32 v29, v29
	v_cvt_pk_f16_f32 v27, v27, v28
	v_cvt_f16_f32_e32 v91, v117
	v_pack_b32_f16 v126, v26, v27
	v_alignbit_b32 v127, v29, v27, 16
	ds_read_b128 v[26:29], v56 offset:15360
	v_cvt_pk_f16_f32 v90, v115, v116
	v_pack_b32_f16 v124, v57, v90
	v_mfma_f32_16x16x32_f16 v[74:77], v[98:101], v[94:97], v[74:77]
	v_alignbit_b32 v125, v91, v90, 16
	s_waitcnt vmcnt(5)
	v_cvt_f16_f32_e32 v130, v30
	v_cvt_pk_f16_f32 v131, v31, v32
	v_cvt_f16_f32_e32 v132, v33
	ds_read_b128 v[90:93], v56 offset:15424
	global_load_dwordx4 v[94:97], v[62:63], off offset:1536
	ds_read_b128 v[98:101], v73 offset:41024
	s_waitcnt lgkmcnt(2)
	v_mfma_f32_16x16x32_f16 v[26:29], v[26:29], v[86:89], v[34:37]
	ds_read_b128 v[30:33], v56 offset:17920
	ds_read_b128 v[102:105], v56 offset:17984
	ds_read_b128 v[106:109], v56 offset:20480
	ds_read_b128 v[110:113], v56 offset:20544
	global_load_dwordx4 v[114:117], v[60:61], off offset:1536
	global_load_dwordx4 v[34:37], v[58:59], off offset:1536
	v_cvt_f16_f32_e32 v57, v22
	v_cvt_pk_f16_f32 v128, v23, v24
	v_cvt_f16_f32_e32 v129, v25
	ds_write2st64_b64 v72, v[118:119], v[120:121] offset1:10
	ds_write2st64_b64 v72, v[122:123], v[124:125] offset0:20 offset1:60
	ds_write_b64 v72, v[126:127] offset:35840
	s_waitcnt lgkmcnt(0)
	s_barrier
	global_load_dwordx4 v[22:25], v[66:67], off offset:1792
	v_mfma_f32_16x16x32_f16 v[74:77], v[30:33], v[86:89], v[74:77]
	global_load_dwordx4 v[30:33], v[64:65], off offset:1792
	v_pack_b32_f16 v118, v57, v128
	v_alignbit_b32 v119, v129, v128, 16
	v_mfma_f32_16x16x32_f16 v[64:67], v[106:109], v[86:89], v[78:81]
	v_pack_b32_f16 v120, v130, v131
	v_alignbit_b32 v121, v132, v131, 16
	s_waitcnt vmcnt(9)
	v_cvt_f16_f32_e32 v38, v38
	v_cvt_f16_f32_e32 v41, v41
	v_cvt_pk_f16_f32 v39, v39, v40
	v_mfma_f32_16x16x32_f16 v[78:81], v[90:93], v[98:101], v[26:29]
	v_pack_b32_f16 v106, v38, v39
	v_alignbit_b32 v107, v41, v39, 16
	s_waitcnt vmcnt(8)
	v_cvt_f16_f32_e32 v38, v42
	v_cvt_f16_f32_e32 v40, v45
	v_cvt_pk_f16_f32 v39, v43, v44
	s_waitcnt vmcnt(7)
	v_cvt_f16_f32_e32 v26, v50
	v_cvt_f16_f32_e32 v27, v53
	v_cvt_pk_f16_f32 v28, v51, v52
	v_mfma_f32_16x16x32_f16 v[50:53], v[102:105], v[98:101], v[74:77]
	v_pack_b32_f16 v102, v26, v28
	v_alignbit_b32 v103, v27, v28, 16
	global_load_dwordx4 v[26:29], v[62:63], off offset:1792
	v_pack_b32_f16 v104, v38, v39
	s_waitcnt vmcnt(7)
	v_cvt_f16_f32_e32 v38, v46
	v_alignbit_b32 v105, v40, v39, 16
	v_cvt_f16_f32_e32 v39, v49
	s_waitcnt vmcnt(6)
	v_cvt_f16_f32_e32 v44, v82
	v_cvt_pk_f16_f32 v40, v47, v48
	v_cvt_pk_f16_f32 v48, v83, v84
	v_pack_b32_f16 v38, v38, v40
	v_alignbit_b32 v39, v39, v40, 16
	ds_read_b128 v[40:43], v56
	v_pack_b32_f16 v108, v44, v48
	v_cvt_f16_f32_e32 v49, v85
	ds_read_b128 v[44:47], v56 offset:2560
	ds_read_b128 v[74:77], v73 offset:30720
	ds_read_b128 v[82:85], v56 offset:5120
	global_load_dwordx4 v[60:63], v[60:61], off offset:1792
	v_mfma_f32_16x16x32_f16 v[64:67], v[110:113], v[98:101], v[64:67]
	ds_read_b128 v[86:89], v56 offset:64
	ds_read_b128 v[90:93], v73 offset:30784
	global_load_dwordx4 v[98:101], v[58:59], off offset:1792
	v_alignbit_b32 v109, v49, v48, 16
	s_waitcnt lgkmcnt(3)
	v_mfma_f32_16x16x32_f16 v[40:43], v[40:43], v[74:77], v[78:81]
	s_waitcnt vmcnt(7)
	v_cvt_pk_f16_f32 v57, v95, v96
	s_nop 0
	ds_read_b128 v[78:81], v56 offset:2624
	v_mfma_f32_16x16x32_f16 v[44:47], v[44:47], v[74:77], v[50:53]
	s_waitcnt vmcnt(6)
	v_cvt_f16_f32_e32 v59, v117
	s_waitcnt vmcnt(5)
	v_cvt_f16_f32_e32 v34, v34
	ds_read_b128 v[48:51], v56 offset:5184
	v_cvt_f16_f32_e32 v52, v94
	v_cvt_f16_f32_e32 v53, v97
	v_cvt_f16_f32_e32 v37, v37
	v_cvt_pk_f16_f32 v35, v35, v36
	s_waitcnt lgkmcnt(4)
	v_mfma_f32_16x16x32_f16 v[64:67], v[82:85], v[74:77], v[64:67]
	v_pack_b32_f16 v52, v52, v57
	v_alignbit_b32 v53, v53, v57, 16
	v_cvt_f16_f32_e32 v57, v114
	s_waitcnt lgkmcnt(2)
	v_mfma_f32_16x16x32_f16 v[40:43], v[86:89], v[90:93], v[40:43]
	ds_write2st64_b64 v72, v[118:119], v[120:121] offset0:30 offset1:40
	ds_write2st64_b64 v72, v[106:107], v[102:103] offset0:50 offset1:80
	ds_write_b64 v72, v[104:105] offset:46080
	v_pack_b32_f16 v86, v34, v35
	v_alignbit_b32 v87, v37, v35, 16
	s_waitcnt lgkmcnt(0)
	s_barrier
	ds_read_b128 v[34:37], v56 offset:15360
	v_cvt_pk_f16_f32 v74, v115, v116
	v_pack_b32_f16 v58, v57, v74
	v_alignbit_b32 v59, v59, v74, 16
	v_mfma_f32_16x16x32_f16 v[48:51], v[48:51], v[90:93], v[64:67]
	s_nop 2
	ds_read_b128 v[64:67], v56 offset:17920
	ds_read_b128 v[74:77], v73 offset:40960
	s_waitcnt vmcnt(4)
	v_cvt_f16_f32_e32 v57, v22
	v_cvt_pk_f16_f32 v89, v23, v24
	v_mfma_f32_16x16x32_f16 v[44:47], v[78:81], v[90:93], v[44:47]
	v_cvt_f16_f32_e32 v90, v25
	ds_read_b128 v[22:25], v56 offset:20480
	ds_read_b128 v[78:81], v56 offset:15424
	ds_read_b128 v[82:85], v73 offset:41024
	s_waitcnt vmcnt(3)
	v_cvt_f16_f32_e32 v30, v30
	s_waitcnt lgkmcnt(3)
	v_mfma_f32_16x16x32_f16 v[34:37], v[34:37], v[74:77], v[40:43]
	v_cvt_f16_f32_e32 v33, v33
	v_cvt_pk_f16_f32 v31, v31, v32
	v_pack_b32_f16 v88, v57, v89
	ds_read_b128 v[40:43], v56 offset:17984
	v_mfma_f32_16x16x32_f16 v[44:47], v[64:67], v[74:77], v[44:47]
	ds_read_b128 v[64:67], v56 offset:20544
	v_alignbit_b32 v89, v90, v89, 16
	v_pack_b32_f16 v90, v30, v31
	s_waitcnt lgkmcnt(4)
	v_mfma_f32_16x16x32_f16 v[22:25], v[22:25], v[74:77], v[48:51]
	v_alignbit_b32 v91, v33, v31, 16
	ds_write2st64_b64 v72, v[38:39], v[108:109] offset1:10
	ds_write2st64_b64 v72, v[52:53], v[58:59] offset0:20 offset1:60
	ds_write_b64 v72, v[86:87] offset:35840
	s_waitcnt lgkmcnt(0)
	v_mfma_f32_16x16x32_f16 v[30:33], v[78:81], v[82:85], v[34:37]
	s_barrier
	s_waitcnt vmcnt(2)
	v_cvt_f16_f32_e32 v57, v26
	ds_read_b128 v[34:37], v56
	v_mfma_f32_16x16x32_f16 v[38:41], v[40:43], v[82:85], v[44:47]
	s_nop 2
	ds_read_b128 v[42:45], v56 offset:2560
	ds_read_b128 v[46:49], v73 offset:30720
	v_cvt_pk_f16_f32 v58, v27, v28
	v_cvt_f16_f32_e32 v59, v29
	v_mfma_f32_16x16x32_f16 v[22:25], v[64:67], v[82:85], v[22:25]
	ds_read_b128 v[50:53], v56 offset:5120
	ds_read_b128 v[64:67], v56 offset:64
	ds_read_b128 v[74:77], v73 offset:30784
	ds_read_b128 v[26:29], v56 offset:2624
	s_waitcnt lgkmcnt(4)
	v_mfma_f32_16x16x32_f16 v[30:33], v[34:37], v[46:49], v[30:33]
	v_mfma_f32_16x16x32_f16 v[34:37], v[42:45], v[46:49], v[38:41]
	s_waitcnt vmcnt(1)
	v_cvt_f16_f32_e32 v44, v60
	v_cvt_f16_f32_e32 v45, v63
	v_pack_b32_f16 v42, v57, v58
	s_waitcnt lgkmcnt(3)
	v_mfma_f32_16x16x32_f16 v[22:25], v[50:53], v[46:49], v[22:25]
	v_cvt_pk_f16_f32 v46, v61, v62
	ds_read_b128 v[38:41], v56 offset:5184
	v_pack_b32_f16 v44, v44, v46
	v_alignbit_b32 v45, v45, v46, 16
	s_waitcnt vmcnt(0)
	v_cvt_f16_f32_e32 v46, v98
	s_waitcnt lgkmcnt(1)
	v_mfma_f32_16x16x32_f16 v[26:29], v[26:29], v[74:77], v[34:37]
	v_alignbit_b32 v43, v59, v58, 16
	ds_write2st64_b64 v72, v[88:89], v[90:91] offset0:30 offset1:40
	ds_write2st64_b64 v72, v[42:43], v[44:45] offset0:50 offset1:80
	v_cvt_f16_f32_e32 v35, v101
	v_cvt_pk_f16_f32 v36, v99, v100
	v_pack_b32_f16 v34, v46, v36
	v_mfma_f32_16x16x32_f16 v[30:33], v[64:67], v[74:77], v[30:33]
	v_alignbit_b32 v35, v35, v36, 16
	ds_write_b64 v72, v[34:35] offset:46080
	s_waitcnt lgkmcnt(0)
	s_barrier
	ds_read_b128 v[34:37], v56 offset:15360
	v_mfma_f32_16x16x32_f16 v[22:25], v[38:41], v[74:77], v[22:25]
	ds_read_b128 v[38:41], v73 offset:40960
	ds_read_b128 v[42:45], v56 offset:15424
	ds_read_b128 v[46:49], v73 offset:41024
	s_waitcnt lgkmcnt(2)
	v_mfma_f32_16x16x32_f16 v[30:33], v[34:37], v[38:41], v[30:33]
	ds_read_b128 v[34:37], v56 offset:17920
	ds_read_b128 v[50:53], v56 offset:17984
	s_waitcnt lgkmcnt(2)
	v_mfma_f32_16x16x32_f16 v[30:33], v[42:45], v[46:49], v[30:33]
	s_waitcnt lgkmcnt(1)
	v_mfma_f32_16x16x32_f16 v[26:29], v[34:37], v[38:41], v[26:29]
	ds_read_b128 v[34:37], v56 offset:20480
	ds_read_b128 v[56:59], v56 offset:20544
	s_waitcnt vmcnt(0)
	s_waitcnt lgkmcnt(0)
	s_nop 2
	v_add_f32_e32 v2, v30, v69
	v_mfma_f32_16x16x32_f16 v[26:29], v[50:53], v[46:49], v[26:29]
	v_cvt_f16_f32_e32 v2, v2
	v_add_f32_e32 v3, v31, v69
	v_cvt_f16_f32_e32 v3, v3
	v_mfma_f32_16x16x32_f16 v[22:25], v[34:37], v[38:41], v[22:25]
	v_add_f32_e32 v4, v32, v69
	v_cvt_f16_f32_e32 v4, v4
	v_add_f32_e32 v5, v33, v69
	v_cvt_f16_f32_e32 v5, v5
	s_barrier
	ds_write_b16 v1, v2
	ds_write_b16 v1, v3 offset:160
	ds_write_b16 v1, v4 offset:320
	ds_write_b16 v1, v5 offset:480
	v_add_f32_e32 v2, v26, v69
	v_mfma_f32_16x16x32_f16 v[22:25], v[56:59], v[46:49], v[22:25]
	v_cvt_f16_f32_e32 v2, v2
	v_add_f32_e32 v3, v27, v69
	v_cvt_f16_f32_e32 v3, v3
	v_add_f32_e32 v4, v28, v69
	v_cvt_f16_f32_e32 v4, v4
	v_add_f32_e32 v5, v29, v69
	v_cvt_f16_f32_e32 v5, v5
	ds_write_b16 v1, v2 offset:2560
	ds_write_b16 v1, v3 offset:2720
	ds_write_b16 v1, v4 offset:2880
	ds_write_b16 v1, v5 offset:3040
	v_add_f32_e32 v2, v22, v69
	v_cvt_f16_f32_e32 v2, v2
	v_add_f32_e32 v3, v23, v69
	v_cvt_f16_f32_e32 v3, v3
	v_add_f32_e32 v4, v24, v69
	v_cvt_f16_f32_e32 v4, v4
	v_add_f32_e32 v5, v25, v69
	v_cvt_f16_f32_e32 v5, v5
	ds_write_b16 v1, v2 offset:5120
	ds_write_b16 v1, v3 offset:5280
	ds_write_b16 v1, v4 offset:5440
	ds_write_b16 v1, v5 offset:5600
	v_and_b32_e32 v2, 7, v0
	v_mul_u32_u24_e32 v10, 12, v2
	v_mul_u32_u24_e32 v2, 0x3c0, v2
	v_lshrrev_b32_e32 v1, 3, v0
	v_lshlrev_b32_e32 v2, 1, v2
	v_lshl_add_u32 v3, v1, 1, v2
	s_waitcnt lgkmcnt(0)
	s_barrier
	ds_read_u16 v2, v3
	ds_read_u16 v4, v3 offset:160
	ds_read_u16 v5, v3 offset:320
	ds_read_u16 v6, v3 offset:480
	ds_read_u16 v7, v3 offset:640
	ds_read_u16 v8, v3 offset:800
	ds_read_u16 v9, v3 offset:960
	ds_read_u16 v11, v3 offset:1120
	ds_read_u16 v12, v3 offset:1280
	ds_read_u16 v13, v3 offset:1440
	ds_read_u16 v14, v3 offset:1600
	ds_read_u16 v15, v3 offset:1760
	v_lshl_or_b32 v1, s18, 9, v1
	s_waitcnt lgkmcnt(10)
	v_lshl_or_b32 v2, v4, 16, v2
	s_waitcnt lgkmcnt(6)
	v_lshl_or_b32 v4, v8, 16, v7
	v_or_b32_e32 v1, s20, v1
	v_mov_b32_e32 v8, s19
	v_mad_u32_u24 v54, v1, s15, v8
	v_lshl_or_b32 v3, v6, 16, v5
	s_waitcnt lgkmcnt(4)
	v_lshl_or_b32 v5, v11, 16, v9
	v_lshl_add_u64 v[8:9], v[54:55], 1, s[12:13]
	v_lshlrev_b32_e32 v54, 1, v10
	v_lshl_add_u64 v[8:9], v[8:9], 0, v[54:55]
	s_waitcnt lgkmcnt(2)
	v_lshl_or_b32 v6, v13, 16, v12
	s_waitcnt lgkmcnt(0)
	v_lshl_or_b32 v7, v15, 16, v14
	global_store_dwordx4 v[8:9], v[2:5], off
	global_store_dwordx2 v[8:9], v[6:7], off offset:16
	s_mov_b64 s[12:13], 0

.LBB0_10:
	s_or_b64 exec, exec, s[8:9]
	v_max_f32_e32 v9, v9, v9
	v_max_f32_e32 v8, v8, v8
	v_max_f32_e32 v5, v5, v5
	v_max_f32_e32 v4, v4, v4
	v_max_f32_e32 v8, v8, v9
	v_max_f32_e32 v4, v4, v5
	v_max3_f32 v6, v6, v7, v8
	v_max3_f32 v2, v2, v3, v4
	v_max3_f32 v2, v6, 0, v2
	s_nop 1
	v_max_f32_dpp v3, v2, v2 quad_perm:[1,0,3,2] row_mask:0xf bank_mask:0xf
	s_nop 1
	v_max_f32_dpp v2, v3, v3 quad_perm:[2,3,0,1] row_mask:0xf bank_mask:0xf
	s_nop 1
	v_max_f32_dpp v3, v2, v2 row_ror:4 row_mask:0xf bank_mask:0xf
	s_nop 1
	v_max_f32_dpp v2, v3, v3 row_ror:8 row_mask:0xf bank_mask:0xf
	s_nop 1
	v_readlane_b32 s80, v2, 0
	v_readlane_b32 s81, v2, 16
	v_readlane_b32 s82, v2, 32
	v_readlane_b32 s83, v2, 48
	s_nop 1
	v_mov_b32_e32 v2, s80
	s_nop 0
	v_max_f32_e32 v2, s81, v2
	v_max_f32_e32 v2, s82, v2
	v_max_f32_e32 v2, s83, v2
	v_mov_b32_e32 v1, v2
	v_cmp_eq_u32_e32 vcc, 0, v17
	s_and_saveexec_b64 s[8:9], vcc
	s_cbranch_execz .LBB0_12
	v_lshrrev_b32_e32 v3, 6, v0
	s_waitcnt lgkmcnt(0)
	v_max_f32_e32 v1, v1, v1
	v_max_f32_e32 v2, v2, v2
	v_lshlrev_b32_e32 v3, 2, v3
	v_max_f32_e32 v1, v2, v1
	ds_write_b32 v3, v1 offset:51200

.LBB0_16:
	s_andn2_b64 vcc, exec, s[8:9]
	s_cbranch_vccnz .LBB0_27
	v_lshlrev_b32_e32 v24, 2, v0
	v_mov_b32_e32 v25, 0
	v_lshrrev_b32_e32 v1, 2, v0
	s_load_dwordx4 s[12:15], s[0:1], 0x48
	s_load_dwordx4 s[8:11], s[0:1], 0x18
	s_load_dwordx2 s[18:19], s[0:1], 0x0
	v_and_b32_e32 v26, 15, v0
	s_waitcnt lgkmcnt(0)
	v_lshl_add_u64 v[2:3], s[6:7], 0, v[24:25]
	v_lshl_add_u64 v[4:5], s[16:17], 0, v[24:25]
	v_cmp_gt_u32_e32 vcc, 64, v0
	v_and_b32_e32 v18, 48, v1
	v_or_b32_e32 v1, v18, v26
	v_cndmask_b32_e32 v3, v5, v3, vcc
	v_cndmask_b32_e32 v2, v4, v2, vcc
	v_bfe_u32 v23, v0, 4, 2
	global_load_dword v22, v[2:3], off
	v_lshlrev_b32_e32 v2, 8, v1
	v_mov_b32_e32 v3, v25
	v_lshl_add_u64 v[2:3], s[12:13], 0, v[2:3]
	v_lshlrev_b32_e32 v4, 5, v23
	v_mov_b32_e32 v5, v25
	s_lshl_b32 s3, s2, 1
	v_lshl_add_u64 v[10:11], v[2:3], 0, v[4:5]
	s_bfe_u32 s21, s2, 0x10002
	s_lshr_b32 s20, s2, 4
	s_and_b32 s3, s3, 6
	s_bfe_u32 s2, s2, 0x10003
	global_load_dwordx4 v[6:9], v[10:11], off
	v_lshl_add_u64 v[2:3], v[10:11], 0, 16
	s_mov_b64 s[6:7], 0x80
	s_or_b32 s3, s2, s3
	s_lshl_b32 s2, s20, 6
	s_mul_i32 s22, s21, 0x180
	global_load_dwordx4 v[14:17], v[2:3], off
	v_lshl_add_u64 v[2:3], v[10:11], 0, s[6:7]
	s_mov_b64 s[6:7], 0x90
	s_add_i32 s22, s22, s2
	s_lshl_b32 s21, s21, 3
	v_lshl_add_u64 v[10:11], v[10:11], 0, s[6:7]
	v_lshlrev_b32_e32 v28, 2, v18
	v_mov_b32_e32 v29, v25
	s_lshl_b32 s6, s3, 8
	global_load_dwordx4 v[2:5], v[2:3], off
	v_lshl_add_u64 v[30:31], s[14:15], 0, v[28:29]
	v_and_b32_e32 v64, 48, v0
	v_mov_b32_e32 v65, v25
	s_add_u32 s6, s10, s6
	global_load_dwordx4 v[10:13], v[10:11], off
	v_lshl_add_u64 v[18:19], v[30:31], 0, v[64:65]
	s_addc_u32 s7, s11, 0
	global_load_dwordx4 v[18:21], v[18:19], off
	v_lshlrev_b32_e32 v32, 2, v26
	v_mov_b32_e32 v33, v25
	v_lshl_add_u64 v[28:29], s[6:7], 0, v[28:29]
	v_lshrrev_b32_e32 v60, 4, v0
	v_lshl_add_u64 v[30:31], v[30:31], 0, v[32:33]
	global_load_dword v96, v[30:31], off
	v_lshl_add_u64 v[28:29], v[28:29], 0, v[32:33]
	v_or_b32_e32 v27, s22, v60
	global_load_dword v97, v[28:29], off
	v_lshlrev_b32_e32 v28, 11, v27
	v_mov_b32_e32 v29, v25
	v_and_b32_e32 v61, 60, v24
	v_lshl_add_u64 v[28:29], s[18:19], 0, v[28:29]
	v_lshlrev_b32_e32 v24, 2, v61
	v_lshl_add_u64 v[88:89], v[28:29], 0, v[24:25]
	global_load_dwordx4 v[28:31], v[88:89], off
	s_mov_b32 s6, 0x10000
	v_add_co_u32_e32 v90, vcc, s6, v88
	v_lshlrev_b32_e32 v27, 9, v60
	s_nop 0
	v_addc_co_u32_e32 v91, vcc, 0, v89, vcc
	global_load_dwordx4 v[32:35], v[90:91], off
	v_lshl_or_b32 v36, s3, 15, v27
	v_mov_b32_e32 v37, v25
	v_lshl_add_u64 v[36:37], v[36:37], 2, s[8:9]
	v_lshl_add_u64 v[92:93], v[36:37], 0, v[24:25]
	global_load_dwordx4 v[36:39], v[92:93], off
	v_add_co_u32_e32 v94, vcc, s6, v92
	v_lshrrev_b32_e32 v24, 3, v0
	s_nop 0
	v_addc_co_u32_e32 v95, vcc, 0, v93, vcc
	global_load_dwordx4 v[40:43], v[94:95], off
	global_load_dwordx4 v[44:47], v[88:89], off offset:256
	global_load_dwordx4 v[48:51], v[90:91], off offset:256
	global_load_dwordx4 v[52:55], v[92:93], off offset:256
	global_load_dwordx4 v[56:59], v[94:95], off offset:256
	v_and_b32_e32 v24, 32, v24
	v_or_b32_e32 v62, v24, v26
	s_movk_i32 s6, 0xa0
	v_mad_u32_u24 v99, v62, s6, v64
	v_mad_u32_u24 v100, v1, s6, v64
	v_lshlrev_b32_e32 v23, 2, v23
	s_load_dwordx2 s[0:1], s[0:1], 0x68
	s_or_b32 s6, s3, s21
	v_cmp_lt_u32_e32 vcc, 63, v0
	s_waitcnt vmcnt(7)
	v_cvt_f16_f32_e32 v27, v28
	v_cvt_f16_f32_e32 v28, v31
	v_cvt_pk_f16_f32 v29, v29, v30
	v_pack_b32_f16 v26, v27, v29
	v_alignbit_b32 v27, v28, v29, 16
	v_mul_u32_u24_e32 v28, 0xa0, v60
	s_waitcnt vmcnt(6)
	v_cvt_f16_f32_e32 v29, v32
	v_cvt_f16_f32_e32 v30, v35
	v_cvt_pk_f16_f32 v31, v33, v34
	v_lshl_add_u32 v98, v61, 1, v28
	v_pack_b32_f16 v28, v29, v31
	v_alignbit_b32 v29, v30, v31, 16
	s_waitcnt vmcnt(5)
	v_cvt_f16_f32_e32 v30, v36
	ds_write2st64_b64 v98, v[26:27], v[28:29] offset1:10
	v_cvt_pk_f16_f32 v27, v37, v38
	v_cvt_f16_f32_e32 v28, v39
	v_pack_b32_f16 v26, v30, v27
	s_waitcnt vmcnt(4)
	v_cvt_f16_f32_e32 v29, v40
	v_cvt_f16_f32_e32 v30, v43
	v_cvt_pk_f16_f32 v31, v41, v42
	v_alignbit_b32 v27, v28, v27, 16
	v_pack_b32_f16 v28, v29, v31
	v_alignbit_b32 v29, v30, v31, 16
	ds_write2st64_b64 v98, v[26:27], v[28:29] offset0:60 offset1:70
	global_load_dwordx4 v[26:29], v[88:89], off offset:512
	global_load_dwordx4 v[30:33], v[90:91], off offset:512
	global_load_dwordx4 v[34:37], v[92:93], off offset:512
	global_load_dwordx4 v[38:41], v[94:95], off offset:512
	s_waitcnt vmcnt(7)
	v_cvt_f16_f32_e32 v42, v44
	v_cvt_pk_f16_f32 v43, v45, v46
	v_cvt_f16_f32_e32 v44, v47
	s_waitcnt vmcnt(6)
	v_cvt_f16_f32_e32 v45, v48
	v_cvt_f16_f32_e32 v47, v51
	v_cvt_pk_f16_f32 v46, v49, v50
	s_waitcnt vmcnt(5)
	v_cvt_f16_f32_e32 v48, v52
	v_cvt_pk_f16_f32 v49, v53, v54
	v_cvt_f16_f32_e32 v50, v55
	s_waitcnt vmcnt(4)
	v_cvt_f16_f32_e32 v51, v56
	v_cvt_f16_f32_e32 v53, v59
	v_cvt_pk_f16_f32 v52, v57, v58
	v_pack_b32_f16 v42, v42, v43
	v_alignbit_b32 v43, v44, v43, 16
	v_pack_b32_f16 v44, v45, v46
	v_alignbit_b32 v45, v47, v46, 16
	s_waitcnt lgkmcnt(0)
	s_barrier
	ds_read_b128 v[60:63], v99
	ds_read_b128 v[64:67], v100 offset:30720
	ds_read_b128 v[68:71], v99 offset:64
	ds_read_b128 v[72:75], v100 offset:30784
	ds_read_b128 v[76:79], v99 offset:2560
	ds_read_b128 v[80:83], v99 offset:2624
	v_pack_b32_f16 v46, v48, v49
	v_alignbit_b32 v47, v50, v49, 16
	v_pack_b32_f16 v48, v51, v52
	v_alignbit_b32 v49, v53, v52, 16
	ds_write2st64_b64 v98, v[42:43], v[44:45] offset0:20 offset1:30
	ds_write2st64_b64 v98, v[46:47], v[48:49] offset0:80 offset1:90
	global_load_dwordx4 v[42:45], v[88:89], off offset:768
	global_load_dwordx4 v[46:49], v[90:91], off offset:768
	global_load_dwordx4 v[50:53], v[92:93], off offset:768
	global_load_dwordx4 v[54:57], v[94:95], off offset:768
	s_waitcnt lgkmcnt(6)
	v_mfma_f32_16x16x32_f16 v[60:63], v[60:63], v[64:67], 0
	s_waitcnt lgkmcnt(0)
	s_barrier
	v_mfma_f32_16x16x32_f16 v[60:63], v[68:71], v[72:75], v[60:63]
	ds_read_b128 v[68:71], v99 offset:10240
	s_waitcnt vmcnt(7)
	v_cvt_f16_f32_e32 v26, v26
	v_mfma_f32_16x16x32_f16 v[64:67], v[76:79], v[64:67], 0
	v_cvt_pk_f16_f32 v27, v27, v28
	v_cvt_f16_f32_e32 v28, v29
	s_waitcnt vmcnt(6)
	v_cvt_f16_f32_e32 v29, v30
	v_cvt_pk_f16_f32 v30, v31, v32
	v_cvt_f16_f32_e32 v31, v33
	s_waitcnt vmcnt(5)
	v_cvt_f16_f32_e32 v32, v34
	v_cvt_pk_f16_f32 v33, v35, v36
	v_cvt_f16_f32_e32 v34, v37
	s_waitcnt vmcnt(4)
	v_cvt_f16_f32_e32 v35, v38
	v_cvt_f16_f32_e32 v37, v41
	v_mfma_f32_16x16x32_f16 v[64:67], v[80:83], v[72:75], v[64:67]
	ds_read_b128 v[72:75], v100 offset:40960
	ds_read_b128 v[76:79], v99 offset:10304
	ds_read_b128 v[80:83], v100 offset:41024
	v_cvt_pk_f16_f32 v36, v39, v40
	v_pack_b32_f16 v26, v26, v27
	v_alignbit_b32 v27, v28, v27, 16
	v_pack_b32_f16 v28, v29, v30
	v_alignbit_b32 v29, v31, v30, 16
	s_waitcnt lgkmcnt(2)
	v_mfma_f32_16x16x32_f16 v[58:61], v[68:71], v[72:75], v[60:63]
	ds_read_b128 v[68:71], v99 offset:12800
	ds_read_b128 v[84:87], v99 offset:12864
	v_pack_b32_f16 v30, v32, v33
	v_alignbit_b32 v31, v34, v33, 16
	v_pack_b32_f16 v32, v35, v36
	v_alignbit_b32 v33, v37, v36, 16
	ds_write2st64_b64 v98, v[26:27], v[28:29] offset1:10
	ds_write2st64_b64 v98, v[30:31], v[32:33] offset0:60 offset1:70
	global_load_dwordx4 v[26:29], v[88:89], off offset:1024
	global_load_dwordx4 v[30:33], v[90:91], off offset:1024
	global_load_dwordx4 v[34:37], v[92:93], off offset:1024
	global_load_dwordx4 v[38:41], v[94:95], off offset:1024
	s_waitcnt lgkmcnt(3)
	v_mfma_f32_16x16x32_f16 v[62:65], v[68:71], v[72:75], v[64:67]
	s_waitcnt lgkmcnt(0)
	s_barrier
	s_nop 0
	ds_read_b128 v[66:69], v99
	s_waitcnt vmcnt(7)
	v_cvt_f16_f32_e32 v42, v42
	v_cvt_pk_f16_f32 v43, v43, v44
	v_cvt_f16_f32_e32 v44, v45
	s_waitcnt vmcnt(6)
	v_cvt_f16_f32_e32 v45, v46
	v_cvt_pk_f16_f32 v46, v47, v48
	v_cvt_f16_f32_e32 v47, v49
	v_mfma_f32_16x16x32_f16 v[58:61], v[76:79], v[80:83], v[58:61]
	s_waitcnt vmcnt(5)
	v_cvt_f16_f32_e32 v48, v50
	v_cvt_pk_f16_f32 v49, v51, v52
	v_cvt_f16_f32_e32 v50, v53
	s_waitcnt vmcnt(4)
	v_cvt_f16_f32_e32 v51, v54
	v_cvt_f16_f32_e32 v53, v57
	v_mfma_f32_16x16x32_f16 v[62:65], v[84:87], v[80:83], v[62:65]
	ds_read_b128 v[70:73], v100 offset:30720
	ds_read_b128 v[74:77], v99 offset:64
	ds_read_b128 v[78:81], v100 offset:30784
	v_cvt_pk_f16_f32 v52, v55, v56
	v_pack_b32_f16 v42, v42, v43
	v_alignbit_b32 v43, v44, v43, 16
	v_pack_b32_f16 v44, v45, v46
	v_alignbit_b32 v45, v47, v46, 16
	s_waitcnt lgkmcnt(2)
	v_mfma_f32_16x16x32_f16 v[58:61], v[66:69], v[70:73], v[58:61]
	ds_read_b128 v[66:69], v99 offset:2560
	ds_read_b128 v[82:85], v99 offset:2624
	v_pack_b32_f16 v46, v48, v49
	v_alignbit_b32 v47, v50, v49, 16
	v_pack_b32_f16 v48, v51, v52
	v_alignbit_b32 v49, v53, v52, 16
	ds_write2st64_b64 v98, v[42:43], v[44:45] offset0:20 offset1:30
	ds_write2st64_b64 v98, v[46:47], v[48:49] offset0:80 offset1:90
	global_load_dwordx4 v[42:45], v[88:89], off offset:1280
	global_load_dwordx4 v[46:49], v[90:91], off offset:1280
	global_load_dwordx4 v[50:53], v[92:93], off offset:1280
	global_load_dwordx4 v[54:57], v[94:95], off offset:1280
	s_waitcnt lgkmcnt(3)
	v_mfma_f32_16x16x32_f16 v[62:65], v[66:69], v[70:73], v[62:65]
	s_waitcnt lgkmcnt(0)
	s_barrier
	ds_read_b128 v[66:69], v99 offset:10240
	v_mfma_f32_16x16x32_f16 v[58:61], v[74:77], v[78:81], v[58:61]
	s_waitcnt vmcnt(7)
	v_cvt_f16_f32_e32 v26, v26
	v_mfma_f32_16x16x32_f16 v[62:65], v[82:85], v[78:81], v[62:65]
	ds_read_b128 v[70:73], v100 offset:40960
	ds_read_b128 v[74:77], v99 offset:10304
	ds_read_b128 v[78:81], v100 offset:41024
	v_cvt_pk_f16_f32 v27, v27, v28
	v_cvt_f16_f32_e32 v28, v29
	s_waitcnt vmcnt(6)
	v_cvt_f16_f32_e32 v29, v30
	v_cvt_pk_f16_f32 v30, v31, v32
	v_cvt_f16_f32_e32 v31, v33
	s_waitcnt vmcnt(5)
	v_cvt_f16_f32_e32 v32, v34
	v_cvt_pk_f16_f32 v33, v35, v36
	v_cvt_f16_f32_e32 v34, v37
	s_waitcnt vmcnt(4)
	v_cvt_f16_f32_e32 v35, v38
	v_cvt_f16_f32_e32 v37, v41
	s_waitcnt lgkmcnt(2)
	v_mfma_f32_16x16x32_f16 v[58:61], v[66:69], v[70:73], v[58:61]
	ds_read_b128 v[66:69], v99 offset:12800
	ds_read_b128 v[82:85], v99 offset:12864
	v_cvt_pk_f16_f32 v36, v39, v40
	v_pack_b32_f16 v26, v26, v27
	v_alignbit_b32 v27, v28, v27, 16
	v_pack_b32_f16 v28, v29, v30
	v_alignbit_b32 v29, v31, v30, 16
	v_pack_b32_f16 v30, v32, v33
	v_alignbit_b32 v31, v34, v33, 16
	v_pack_b32_f16 v32, v35, v36
	v_alignbit_b32 v33, v37, v36, 16
	ds_write2st64_b64 v98, v[26:27], v[28:29] offset1:10
	ds_write2st64_b64 v98, v[30:31], v[32:33] offset0:60 offset1:70
	s_waitcnt lgkmcnt(3)
	v_mfma_f32_16x16x32_f16 v[62:65], v[66:69], v[70:73], v[62:65]
	global_load_dwordx4 v[26:29], v[88:89], off offset:1536
	global_load_dwordx4 v[30:33], v[90:91], off offset:1536
	global_load_dwordx4 v[34:37], v[92:93], off offset:1536
	global_load_dwordx4 v[38:41], v[94:95], off offset:1536
	s_waitcnt lgkmcnt(0)
	s_barrier
	ds_read_b128 v[66:69], v99
	v_mfma_f32_16x16x32_f16 v[58:61], v[74:77], v[78:81], v[58:61]
	s_waitcnt vmcnt(6)
	v_cvt_f16_f32_e32 v49, v49
	s_waitcnt vmcnt(5)
	v_cvt_f16_f32_e32 v50, v50
	v_mfma_f32_16x16x32_f16 v[62:65], v[82:85], v[78:81], v[62:65]
	ds_read_b128 v[70:73], v100 offset:30720
	ds_read_b128 v[74:77], v99 offset:64
	ds_read_b128 v[78:81], v100 offset:30784
	global_load_dwordx4 v[82:85], v[88:89], off offset:1792
	ds_read_b128 v[86:89], v99 offset:2624
	s_waitcnt lgkmcnt(3)
	v_mfma_f32_16x16x32_f16 v[58:61], v[66:69], v[70:73], v[58:61]
	ds_read_b128 v[66:69], v99 offset:2560
	v_cvt_pk_f16_f32 v51, v51, v52
	v_cvt_f16_f32_e32 v52, v53
	s_waitcnt lgkmcnt(0)
	v_mfma_f32_16x16x32_f16 v[62:65], v[66:69], v[70:73], v[62:65]
	global_load_dwordx4 v[66:69], v[90:91], off offset:1792
	v_cvt_f16_f32_e32 v70, v42
	v_cvt_f16_f32_e32 v72, v45
	v_cvt_f16_f32_e32 v73, v46
	v_mfma_f32_16x16x32_f16 v[58:61], v[74:77], v[78:81], v[58:61]
	v_cvt_pk_f16_f32 v71, v43, v44
	v_cvt_pk_f16_f32 v74, v47, v48
	global_load_dwordx4 v[42:45], v[92:93], off offset:1792
	v_pack_b32_f16 v46, v70, v71
	v_alignbit_b32 v47, v72, v71, 16
	v_pack_b32_f16 v48, v73, v74
	v_alignbit_b32 v49, v49, v74, 16
	ds_write2st64_b64 v98, v[46:47], v[48:49] offset0:20 offset1:30
	global_load_dwordx4 v[46:49], v[94:95], off offset:1792
	s_waitcnt vmcnt(8)
	v_cvt_f16_f32_e32 v53, v54
	v_cvt_pk_f16_f32 v54, v55, v56
	v_cvt_f16_f32_e32 v55, v57
	v_pack_b32_f16 v50, v50, v51
	v_alignbit_b32 v51, v52, v51, 16
	v_pack_b32_f16 v52, v53, v54
	v_alignbit_b32 v53, v55, v54, 16
	ds_write2st64_b64 v98, v[50:51], v[52:53] offset0:80 offset1:90
	s_waitcnt lgkmcnt(0)
	s_barrier
	ds_read_b128 v[50:53], v99 offset:10240
	v_mfma_f32_16x16x32_f16 v[54:57], v[86:89], v[78:81], v[62:65]
	s_nop 2
	ds_read_b128 v[62:65], v100 offset:40960
	ds_read_b128 v[70:73], v99 offset:10304
	ds_read_b128 v[74:77], v100 offset:41024
	s_waitcnt vmcnt(7)
	v_cvt_f16_f32_e32 v26, v26
	v_cvt_pk_f16_f32 v27, v27, v28
	v_cvt_f16_f32_e32 v28, v29
	s_waitcnt vmcnt(6)
	v_cvt_f16_f32_e32 v29, v30
	v_cvt_pk_f16_f32 v30, v31, v32
	v_cvt_f16_f32_e32 v31, v33
	s_waitcnt vmcnt(5)
	v_cvt_f16_f32_e32 v32, v34
	v_cvt_pk_f16_f32 v33, v35, v36
	v_cvt_f16_f32_e32 v34, v37
	s_waitcnt vmcnt(4)
	v_cvt_f16_f32_e32 v35, v38
	v_cvt_f16_f32_e32 v37, v41
	s_waitcnt lgkmcnt(2)
	v_mfma_f32_16x16x32_f16 v[50:53], v[50:53], v[62:65], v[58:61]
	s_nop 2
	ds_read_b128 v[58:61], v99 offset:12800
	ds_read_b128 v[78:81], v99 offset:12864
	v_cvt_pk_f16_f32 v36, v39, v40
	v_pack_b32_f16 v26, v26, v27
	v_alignbit_b32 v27, v28, v27, 16
	v_pack_b32_f16 v28, v29, v30
	v_alignbit_b32 v29, v31, v30, 16
	s_waitcnt vmcnt(3)
	v_cvt_f16_f32_e32 v38, v82
	v_cvt_f16_f32_e32 v40, v85
	v_pack_b32_f16 v30, v32, v33
	v_alignbit_b32 v31, v34, v33, 16
	v_pack_b32_f16 v32, v35, v36
	v_alignbit_b32 v33, v37, v36, 16
	ds_write2st64_b64 v98, v[26:27], v[28:29] offset1:10
	ds_write2st64_b64 v98, v[30:31], v[32:33] offset0:60 offset1:70
	s_waitcnt lgkmcnt(0)
	s_barrier
	s_waitcnt vmcnt(2)
	v_cvt_f16_f32_e32 v41, v66
	ds_read_b128 v[26:29], v99
	v_mfma_f32_16x16x32_f16 v[54:57], v[58:61], v[62:65], v[54:57]
	v_cvt_pk_f16_f32 v39, v83, v84
	v_cvt_pk_f16_f32 v58, v67, v68
	v_pack_b32_f16 v62, v38, v39
	v_alignbit_b32 v63, v40, v39, 16
	v_pack_b32_f16 v64, v41, v58
	ds_read_b128 v[34:37], v99 offset:2560
	ds_read_b128 v[38:41], v100 offset:30720
	v_mfma_f32_16x16x32_f16 v[30:33], v[70:73], v[74:77], v[50:53]
	v_cvt_f16_f32_e32 v59, v69
	s_waitcnt vmcnt(1)
	v_cvt_f16_f32_e32 v42, v42
	v_cvt_pk_f16_f32 v43, v43, v44
	v_mfma_f32_16x16x32_f16 v[50:53], v[78:81], v[74:77], v[54:57]
	v_cvt_f16_f32_e32 v44, v45
	v_alignbit_b32 v65, v59, v58, 16
	s_nop 0
	ds_read_b128 v[54:57], v99 offset:64
	ds_read_b128 v[58:61], v100 offset:30784
	s_waitcnt lgkmcnt(2)
	v_mfma_f32_16x16x32_f16 v[26:29], v[26:29], v[38:41], v[30:33]
	v_mfma_f32_16x16x32_f16 v[34:37], v[34:37], v[38:41], v[50:53]
	s_waitcnt vmcnt(0)
	v_cvt_f16_f32_e32 v40, v46
	v_cvt_f16_f32_e32 v41, v49
	ds_read_b128 v[30:33], v99 offset:2624
	v_pack_b32_f16 v38, v42, v43
	v_cvt_pk_f16_f32 v42, v47, v48
	v_alignbit_b32 v39, v44, v43, 16
	v_pack_b32_f16 v40, v40, v42
	v_alignbit_b32 v41, v41, v42, 16
	ds_write2st64_b64 v98, v[62:63], v[64:65] offset0:20 offset1:30
	ds_write2st64_b64 v98, v[38:39], v[40:41] offset0:80 offset1:90
	s_waitcnt lgkmcnt(0)
	s_barrier
	ds_read_b128 v[38:41], v99 offset:10240
	v_mfma_f32_16x16x32_f16 v[26:29], v[54:57], v[58:61], v[26:29]
	v_mfma_f32_16x16x32_f16 v[30:33], v[30:33], v[58:61], v[34:37]
	s_nop 2
	ds_read_b128 v[34:37], v100 offset:40960
	ds_read_b128 v[42:45], v99 offset:10304
	ds_read_b128 v[46:49], v100 offset:41024
	s_waitcnt lgkmcnt(2)
	v_mfma_f32_16x16x32_f16 v[26:29], v[38:41], v[34:37], v[26:29]
	ds_read_b128 v[38:41], v99 offset:12800
	ds_read_b128 v[50:53], v99 offset:12864
	s_waitcnt vmcnt(0)
	s_waitcnt lgkmcnt(0)
	v_mfma_f32_16x16x32_f16 v[26:29], v[42:45], v[46:49], v[26:29]
	v_or_b32_e32 v18, v23, v24
	v_mul_u32_u24_e32 v18, 0xa0, v18
	v_lshl_add_u32 v18, v1, 1, v18
	v_mfma_f32_16x16x32_f16 v[30:33], v[38:41], v[34:37], v[30:33]
	s_barrier
	s_nop 2
	v_add_f32_e32 v19, v26, v97
	v_cvt_f16_f32_e32 v19, v19
	v_mfma_f32_16x16x32_f16 v[30:33], v[50:53], v[46:49], v[30:33]
	v_add_f32_e32 v20, v27, v97
	v_cvt_f16_f32_e32 v20, v20
	v_add_f32_e32 v21, v28, v97
	v_cvt_f16_f32_e32 v21, v21
	v_add_f32_e32 v26, v29, v97
	v_cvt_f16_f32_e32 v26, v26
	ds_write_b16 v18, v19
	ds_write_b16 v18, v20 offset:160
	ds_write_b16 v18, v21 offset:320
	ds_write_b16 v18, v26 offset:480
	v_add_f32_e32 v19, v30, v97
	v_cvt_f16_f32_e32 v19, v19
	v_add_f32_e32 v20, v31, v97
	v_cvt_f16_f32_e32 v20, v20
	v_add_f32_e32 v21, v32, v97
	v_cvt_f16_f32_e32 v21, v21
	v_add_f32_e32 v26, v33, v97
	v_cvt_f16_f32_e32 v26, v26
	ds_write_b16 v18, v19 offset:2560
	ds_write_b16 v18, v20 offset:2720
	ds_write_b16 v18, v21 offset:2880
	ds_write_b16 v18, v26 offset:3040
	s_waitcnt lgkmcnt(0)
	s_barrier
	ds_read_b128 v[18:21], v99
	v_cvt_pk_f16_f32 v17, v16, v17
	v_cvt_pk_f16_f32 v16, v14, v15
	v_cvt_pk_f16_f32 v15, v8, v9
	v_cvt_pk_f16_f32 v14, v6, v7
	ds_read_b128 v[6:9], v99 offset:64
	ds_read_b128 v[26:29], v99 offset:2560
	ds_read_b128 v[30:33], v99 offset:2624
	s_waitcnt lgkmcnt(3)
	v_mfma_f32_16x16x32_f16 v[18:21], v[18:21], v[14:17], 0
	v_cvt_pk_f16_f32 v13, v12, v13
	v_cvt_pk_f16_f32 v12, v10, v11
	v_cvt_pk_f16_f32 v11, v4, v5
	s_waitcnt lgkmcnt(1)
	v_mfma_f32_16x16x32_f16 v[14:17], v[26:29], v[14:17], 0
	v_cvt_pk_f16_f32 v10, v2, v3
	s_nop 1
	v_mfma_f32_16x16x32_f16 v[2:5], v[6:9], v[10:13], v[18:21]
	s_waitcnt lgkmcnt(0)
	v_mfma_f32_16x16x32_f16 v[6:9], v[30:33], v[10:13], v[14:17]
	v_or3_b32 v12, s2, v24, v23
	v_lshlrev_b32_e32 v24, 3, v1
	v_lshl_add_u64 v[10:11], s[0:1], 0, v[24:25]
	s_nop 2
	v_add_f32_e32 v1, v96, v2
	s_mov_b32 s0, 0xc2200000
	v_mov_b32_e32 v14, 0x42200000
	v_med3_f32 v1, v1, s0, v14
	v_mul_f32_e32 v1, 0x4038aa3b, v1
	v_exp_f32_e32 v2, v1
	v_add_f32_e32 v1, v96, v3
	v_med3_f32 v1, v1, s0, v14
	v_mul_f32_e32 v1, 0x4038aa3b, v1
	s_mul_i32 s2, s6, 0xc0
	v_exp_f32_e32 v3, v1
	v_lshrrev_b32_e32 v1, 1, v12
	v_add_u32_e32 v24, s2, v1
	v_add_f32_e32 v1, v96, v4
	v_med3_f32 v1, v1, s0, v14
	v_mul_f32_e32 v1, 0x4038aa3b, v1
	v_exp_f32_e32 v4, v1
	v_add_f32_e32 v1, v96, v5
	v_med3_f32 v1, v1, s0, v14
	v_mul_f32_e32 v1, 0x4038aa3b, v1
	v_exp_f32_e32 v5, v1
	v_add_f32_e32 v1, v96, v6
	v_med3_f32 v1, v1, s0, v14
	v_mul_f32_e32 v1, 0x4038aa3b, v1
	v_exp_f32_e32 v6, v1
	v_add_f32_e32 v1, v96, v7
	v_med3_f32 v1, v1, s0, v14
	v_mul_f32_e32 v1, 0x4038aa3b, v1
	v_lshlrev_b64 v[12:13], 9, v[24:25]
	v_exp_f32_e32 v7, v1
	v_add_f32_e32 v1, v96, v8
	v_lshl_add_u64 v[12:13], v[10:11], 0, v[12:13]
	v_med3_f32 v1, v1, s0, v14
	global_store_dwordx2 v[12:13], v[2:3], off
	v_or_b32_e32 v12, 1, v24
	v_mov_b32_e32 v13, v25
	v_mul_f32_e32 v1, 0x4038aa3b, v1
	v_lshlrev_b64 v[12:13], 9, v[12:13]
	v_exp_f32_e32 v8, v1
	v_add_f32_e32 v1, v96, v9
	v_lshl_add_u64 v[12:13], v[10:11], 0, v[12:13]
	v_med3_f32 v1, v1, s0, v14
	global_store_dwordx2 v[12:13], v[4:5], off
	v_or_b32_e32 v12, 8, v24
	v_mov_b32_e32 v13, v25
	v_mul_f32_e32 v1, 0x4038aa3b, v1
	v_lshlrev_b64 v[12:13], 9, v[12:13]
	v_exp_f32_e32 v9, v1
	v_lshl_add_u64 v[12:13], v[10:11], 0, v[12:13]
	v_or_b32_e32 v24, 9, v24
	global_store_dwordx2 v[12:13], v[6:7], off
	v_lshlrev_b64 v[12:13], 9, v[24:25]
	v_lshl_add_u64 v[10:11], v[10:11], 0, v[12:13]
	global_store_dwordx2 v[10:11], v[8:9], off
	v_mbcnt_lo_u32_b32 v10, -1, 0
	s_and_saveexec_b64 s[0:1], vcc
	s_xor_b64 s[0:1], exec, s[0:1]
	v_mbcnt_hi_u32_b32 v1, -1, v10
	v_and_b32_e32 v10, 64, v1
	v_add_u32_e32 v14, 64, v10
	v_xor_b32_e32 v15, 32, v1
	v_xor_b32_e32 v16, 16, v1
	v_xor_b32_e32 v18, 8, v1
	v_xor_b32_e32 v19, 4, v1
	v_xor_b32_e32 v20, 2, v1
	v_xor_b32_e32 v21, 1, v1
	s_or_saveexec_b64 s[0:1], s[0:1]
	v_and_b32_e32 v17, 63, v0
	s_xor_b64 exec, exec, s[0:1]
	s_cmp_gt_u32 s88, 7
	s_cbranch_scc1 .LBB0_23
	s_cbranch_execz .LBB0_23
	v_mbcnt_hi_u32_b32 v1, -1, v10
	v_and_b32_e32 v10, 64, v1
	v_add_u32_e32 v14, 64, v10
	v_xor_b32_e32 v15, 32, v1
	v_cmp_lt_i32_e32 vcc, v15, v14
	v_and_b32_e32 v23, 0x7fffffff, v22
	v_xor_b32_e32 v16, 16, v1
	v_cndmask_b32_e32 v10, v1, v15, vcc
	v_lshlrev_b32_e32 v11, 2, v10
	ds_bpermute_b32 v10, v11, v22
	ds_bpermute_b32 v11, v11, v23
	v_cmp_lt_i32_e32 vcc, v16, v14
	v_xor_b32_e32 v18, 8, v1
	s_waitcnt lgkmcnt(0)
	v_pk_add_f32 v[10:11], v[22:23], v[10:11]
	v_cndmask_b32_e32 v12, v1, v16, vcc
	v_lshlrev_b32_e32 v13, 2, v12
	ds_bpermute_b32 v12, v13, v10
	ds_bpermute_b32 v13, v13, v11
	v_cmp_lt_i32_e32 vcc, v18, v14
	s_waitcnt lgkmcnt(0)
	v_pk_add_f32 v[10:11], v[10:11], v[12:13]
	v_cndmask_b32_e32 v19, v1, v18, vcc
	v_lshlrev_b32_e32 v19, 2, v19
	ds_bpermute_b32 v12, v19, v10
	ds_bpermute_b32 v13, v19, v11
	v_xor_b32_e32 v19, 4, v1
	v_cmp_lt_i32_e32 vcc, v19, v14
	s_waitcnt lgkmcnt(0)
	v_pk_add_f32 v[10:11], v[10:11], v[12:13]
	v_cndmask_b32_e32 v20, v1, v19, vcc
	v_lshlrev_b32_e32 v20, 2, v20
	ds_bpermute_b32 v12, v20, v10
	ds_bpermute_b32 v13, v20, v11
	v_xor_b32_e32 v20, 2, v1
	v_cmp_lt_i32_e32 vcc, v20, v14
	s_waitcnt lgkmcnt(0)
	v_pk_add_f32 v[10:11], v[10:11], v[12:13]
	v_cndmask_b32_e32 v21, v1, v20, vcc
	v_lshlrev_b32_e32 v21, 2, v21
	ds_bpermute_b32 v12, v21, v10
	ds_bpermute_b32 v13, v21, v11
	v_xor_b32_e32 v21, 1, v1
	v_cmp_lt_i32_e32 vcc, v21, v14
	s_waitcnt lgkmcnt(0)
	v_pk_add_f32 v[10:11], v[10:11], v[12:13]
	v_cndmask_b32_e32 v12, v1, v21, vcc
	v_lshlrev_b32_e32 v13, 2, v12
	ds_bpermute_b32 v12, v13, v10
	ds_bpermute_b32 v13, v13, v11
	v_cmp_eq_u32_e32 vcc, 0, v17
	s_and_saveexec_b64 s[2:3], vcc
	s_cbranch_execz .LBB0_22
	v_mov_b32_e32 v22, 0
	s_waitcnt lgkmcnt(0)
	v_pk_add_f32 v[10:11], v[10:11], v[12:13]
	global_store_dwordx2 v22, v[10:11], s[4:5] offset:1024

.LBB0_23:
	s_or_b64 exec, exec, s[0:1]
	v_max_f32_e32 v3, v3, v3
	v_max_f32_e32 v2, v2, v2
	v_max_f32_e32 v2, v2, v3
	v_max_f32_e32 v3, v5, v5
	v_max_f32_e32 v4, v4, v4
	v_max_f32_e32 v3, v4, v3
	v_max3_f32 v2, v2, 0, v3
	v_max_f32_e32 v3, v7, v7
	v_max_f32_e32 v4, v6, v6
	v_max_f32_e32 v3, v4, v3
	v_max_f32_e32 v4, v9, v9
	v_max_f32_e32 v5, v8, v8
	v_max_f32_e32 v4, v5, v4
	v_max3_f32 v2, v2, v3, v4
	s_nop 1
	v_max_f32_dpp v3, v2, v2 quad_perm:[1,0,3,2] row_mask:0xf bank_mask:0xf
	s_nop 1
	v_max_f32_dpp v2, v3, v3 quad_perm:[2,3,0,1] row_mask:0xf bank_mask:0xf
	s_nop 1
	v_max_f32_dpp v3, v2, v2 row_ror:4 row_mask:0xf bank_mask:0xf
	s_nop 1
	v_max_f32_dpp v2, v3, v3 row_ror:8 row_mask:0xf bank_mask:0xf
	s_nop 1
	v_readlane_b32 s80, v2, 0
	v_readlane_b32 s81, v2, 16
	v_readlane_b32 s82, v2, 32
	v_readlane_b32 s83, v2, 48
	s_nop 1
	v_mov_b32_e32 v2, s80
	s_nop 0
	v_max_f32_e32 v2, s81, v2
	v_max_f32_e32 v2, s82, v2
	v_max_f32_e32 v2, s83, v2
	v_mov_b32_e32 v1, v2
	v_cmp_eq_u32_e32 vcc, 0, v17
	s_and_saveexec_b64 s[0:1], vcc
	s_cbranch_execz .LBB0_25
	v_lshrrev_b32_e32 v3, 6, v0
	s_waitcnt lgkmcnt(0)
	v_max_f32_e32 v1, v1, v1
	v_max_f32_e32 v2, v2, v2
	v_lshlrev_b32_e32 v3, 2, v3
	v_max_f32_e32 v1, v2, v1
	ds_write_b32 v3, v1 offset:51200
